# final_kernel: tabA and record addressing with scalar base + 32-bit offsets instead of 64-bit vector address math (13 fewer VALU per thread)
# speedup vs baseline: 1.0027x; 1.0027x over previous
_Z12final_kernelPK15HIP_vector_typeIiLj2EEPKiPKfS6_S6_S4_Pf:
	s_movk_i32 s3, 0x3e8
	v_lshrrev_b32_e32 v1, 2, v0
	v_cmp_gt_u32_e32 vcc, s3, v0
	v_mov_b64_e32 v[2:3], 0
	v_mov_b32_e32 v34, 0
	v_mov_b32_e32 v35, 0
	s_and_saveexec_b64 s[4:5], vcc
	s_cbranch_execz .LBB2_2
	s_load_dwordx2 s[6:7], s[0:1], 0x8
	s_lshl_b32 s3, s2, 10
	v_lshl_add_u32 v4, v1, 2, s3
	s_waitcnt lgkmcnt(0)
	global_load_dword v2, v4, s[6:7]
	global_load_dword v8, v4, s[6:7] offset:1024
	s_waitcnt vmcnt(0)
	v_sub_u32_e32 v35, v8, v2

.LBB2_4:
	s_or_b64 exec, exec, s[4:5]
	s_load_dwordx2 s[26:27], s[0:1], 0x0
	v_lshlrev_b32_e32 v36, 3, v0
	s_and_saveexec_b64 s[4:5], s[2:3]
	v_mov_b32_e32 v4, 0
	v_mov_b32_e32 v5, v4
	ds_write_b64 v36, v[4:5]
	s_or_b64 exec, exec, s[4:5]
	s_load_dwordx2 s[24:25], s[0:1], 0x10
	v_cmp_eq_u32_e64 s[2:3], 0, v0
	s_and_saveexec_b64 s[4:5], s[2:3]
	v_mov_b32_e32 v4, 0
	ds_write_b32 v4, v4 offset:1568
	s_or_b64 exec, exec, s[4:5]
	v_mul_u32_u24_e32 v26, 0x1f40, v1
	v_mov_b32_e32 v27, 0
	v_max_i32_e32 v1, 1, v35
	v_and_b32_e32 v37, 3, v0
	v_add_u32_e32 v22, v26, v2
	v_add_u32_e32 v6, -1, v1
	v_lshlrev_b32_e32 v1, 1, v37
	v_cndmask_b32_e32 v22, 0, v22, vcc
	v_mov_b32_e32 v23, 0
	v_min_u32_e32 v2, v1, v6
	v_or_b32_e32 v30, 8, v1
	v_or_b32_e32 v25, 16, v1
	v_or_b32_e32 v24, 24, v1
	s_waitcnt lgkmcnt(0)
	v_lshl_add_u64 v[28:29], v[22:23], 3, s[26:27]
	v_add_lshl_u32 v2, v22, v2, 3
	v_min_u32_e32 v4, v30, v6
	v_add_lshl_u32 v4, v22, v4, 3
	global_load_dwordx4 v[14:17], v2, s[26:27]
	global_load_dwordx4 v[10:13], v4, s[26:27]
	v_min_u32_e32 v2, v25, v6
	v_min_u32_e32 v3, v24, v6
	v_add_lshl_u32 v2, v22, v2, 3
	v_add_lshl_u32 v3, v22, v3, 3
	global_load_dwordx4 v[6:9], v2, s[26:27]
	global_load_dwordx4 v[2:5], v3, s[26:27]
	v_cmp_lt_i32_e64 s[16:17], v1, v35
	v_mov_b32_e32 v26, 0
	s_and_saveexec_b64 s[2:3], s[16:17]
	s_cbranch_execz .LBB2_10
	s_waitcnt vmcnt(3)
	v_and_b32_e32 v26, 0x7ffff, v14
	s_mov_b32 s4, 0x7a120
	v_cmp_gt_u32_e32 vcc, s4, v26
	s_nop 1
	v_cndmask_b32_e32 v26, 0, v26, vcc
	v_lshlrev_b32_e32 v26, 2, v26
	global_load_dword v26, v26, s[24:25]
	s_waitcnt vmcnt(0)
	v_mul_f32_e32 v26, v15, v26
